# baseline (speedup 1.0000x reference)
_Z11k_conv_mfmaPKDF16_PKDv8_DF16_PKfS5_S5_S5_S5_PDF16_:
	s_load_dwordx4 s[8:11], s[0:1], 0x0
	s_load_dwordx8 s[36:43], s[0:1], 0x10
	s_load_dwordx4 s[44:47], s[0:1], 0x30
	s_lshr_b32 s6, s2, 1
	v_readfirstlane_b32 s24, v0
	s_and_b32 s25, s2, 3
	s_and_b32 s3, s6, 2
	s_lshr_b32 s4, s2, 7
	s_lshr_b32 s2, s2, 3
	s_lshr_b32 s23, s24, 6
	s_add_i32 s7, s3, s4
	s_and_b32 s22, s2, 12
	s_mul_i32 s2, s25, 0x65400
	v_and_b32_e32 v1, 63, v0
	s_waitcnt lgkmcnt(0)
	s_lshl_b32 s21, s7, 2
	s_and_b32 s20, s6, 12
	s_add_i32 s12, s20, -1
	v_mul_u32_u24_e32 v16, 0xccd, v1
	v_add_u32_e32 v17, 64, v1
	v_lshrrev_b32_e32 v16, 16, v16
	v_mul_u32_u24_e32 v18, 0xccd, v17
	v_lshlrev_b32_e32 v19, 4, v1
	v_lshrrev_b32_e32 v18, 16, v18
	v_lshlrev_b32_e32 v21, 4, v17
	v_lshl_add_u32 v20, v16, 5, v19
	v_lshl_add_u32 v22, v18, 5, v21
	v_add_u32_e32 v23, s12, v16
	v_add_u32_e32 v17, s12, v18
	v_cmp_gt_u32_e64 s[14:15], 16, v23
	v_cmp_gt_u32_e64 s[16:17], 16, v17
	v_cmp_gt_u32_e64 s[18:19], 56, v1
	v_mov_b64_e32 v[24:25], 0
	v_mov_b64_e32 v[26:27], 0
	v_mov_b64_e32 v[28:29], 0
	v_mov_b64_e32 v[30:31], 0
	v_mov_b64_e32 v[32:33], 0
	v_mov_b64_e32 v[34:35], 0
	v_mov_b64_e32 v[36:37], 0
	v_mov_b64_e32 v[38:39], 0
	v_mov_b64_e32 v[40:41], 0
	v_mov_b64_e32 v[42:43], 0
	v_mov_b64_e32 v[44:45], 0
	v_mov_b64_e32 v[46:47], 0
	v_mov_b64_e32 v[102:103], 0
	v_mov_b64_e32 v[104:105], 0
	v_mov_b64_e32 v[106:107], 0
	v_mov_b64_e32 v[108:109], 0
	v_mov_b64_e32 v[110:111], 0
	v_mov_b64_e32 v[112:113], 0
	v_mov_b64_e32 v[114:115], 0
	v_mov_b64_e32 v[116:117], 0
	s_and_b64 s[16:17], s[16:17], s[18:19]
	s_add_i32 s26, s23, 0
	s_mul_i32 s27, s26, 43
	s_lshr_b32 s27, s27, 8
	s_mul_i32 s28, s27, 6
	s_sub_i32 s28, s26, s28
	s_add_i32 s27, s27, s21
	s_add_i32 s28, s28, s22
	s_add_i32 s27, s27, -1
	s_add_i32 s28, s28, -1
	s_or_b32 s29, s27, s28
	s_cmp_lt_u32 s29, 16
	s_cbranch_scc0 .Lmy_conv_skip0
	s_lshl_b32 s27, s27, 8
	s_lshl_b32 s28, s28, 4
	s_add_i32 s27, s27, s28
	s_add_i32 s27, s27, s12
	s_mulk_i32 s27, 0x140
	s_ashr_i32 s28, s27, 31
	s_add_u32 s34, s8, s27
	s_addc_u32 s35, s9, s28
	s_mov_b64 exec, s[14:15]
	global_load_dwordx4 v[24:27], v19, s[34:35]
	s_mov_b64 exec, s[16:17]
	global_load_dwordx4 v[28:31], v21, s[34:35]
	s_mov_b64 exec, -1

.Lmy_conv_skip4:
	v_and_b32_e32 v135, 15, v0
	s_mul_i32 s25, s25, 40
	v_add_lshl_u32 v10, v135, s25, 2
	v_or_b32_e32 v11, 32, v135
	v_cmp_gt_u32_e32 vcc, 40, v11
	global_load_dword v164, v10, s[44:45]
	global_load_dword v140, v10, s[36:37]
	global_load_dword v141, v10, s[42:43]
	global_load_dword v134, v10, s[40:41]
	global_load_dword v138, v10, s[38:39] offset:64
	global_load_dword v139, v10, s[36:37] offset:64
	global_load_dword v165, v10, s[44:45] offset:64
	v_cndmask_b32_e32 v11, 0, v11, vcc
	v_add_lshl_u32 v11, v11, s25, 2
	global_load_dword v142, v11, s[36:37]
	global_load_dword v143, v11, s[42:43]
	global_load_dword v136, v11, s[40:41]
	global_load_dword v166, v11, s[44:45]
	global_load_dword v146, v10, s[38:39]
	global_load_dword v144, v11, s[38:39]
	global_load_dword v145, v10, s[42:43] offset:64
	global_load_dword v137, v10, s[40:41] offset:64
	s_add_u32 s4, s10, s2
	v_mov_b32_e32 v10, 0
	s_addc_u32 s5, s11, 0
	v_lshlrev_b32_e32 v2, 4, v1
	v_mov_b32_e32 v3, v10
	v_lshl_add_u64 v[130:131], s[4:5], 0, v[2:3]
	v_and_b32_e32 v2, 8, v0
	v_lshlrev_b32_e32 v2, 4, v2
	s_mul_i32 s2, s23, 0xc0
	s_mov_b32 s3, 0
	v_sub_co_u32_e32 v132, vcc, v130, v2
	s_ashr_i32 s5, s2, 31
	s_mov_b32 s4, s2
	v_subbrev_co_u32_e32 v133, vcc, 0, v131, vcc
	v_lshl_add_u64 v[12:13], s[2:3], 4, v[130:131]
	s_lshl_b64 s[4:5], s[4:5], 4
	v_lshl_add_u64 v[14:15], v[130:131], 0, s[4:5]
	global_load_dwordx4 v[2:5], v[12:13], off
	global_load_dwordx4 v[6:9], v[14:15], off offset:1024
	v_lshl_add_u64 v[12:13], v[132:133], 0, s[4:5]
	s_add_i32 s4, s2, 0x600
	s_mov_b32 s5, s3
	v_lshl_add_u64 v[14:15], s[4:5], 4, v[130:131]
	s_ashr_i32 s5, s4, 31
	s_lshl_b64 s[4:5], s[4:5], 4
	global_load_dwordx4 v[98:101], v[12:13], off offset:2048
	global_load_dwordx4 v[86:89], v[14:15], off
	v_lshl_add_u64 v[12:13], v[130:131], 0, s[4:5]
	v_lshl_add_u64 v[14:15], v[132:133], 0, s[4:5]
	s_add_i32 s4, s2, 0xc00
	s_mov_b32 s5, s3
	global_load_dwordx4 v[90:93], v[12:13], off offset:1024
	global_load_dwordx4 v[94:97], v[14:15], off offset:2048
	v_lshl_add_u64 v[12:13], s[4:5], 4, v[130:131]
	s_ashr_i32 s5, s4, 31
	s_lshl_b64 s[4:5], s[4:5], 4
	v_lshl_add_u64 v[14:15], v[130:131], 0, s[4:5]
	global_load_dwordx4 v[74:77], v[12:13], off
	global_load_dwordx4 v[78:81], v[14:15], off offset:1024
	v_lshl_add_u64 v[12:13], v[132:133], 0, s[4:5]
	s_add_i32 s4, s2, 0x1200
	s_mov_b32 s5, s3
	v_lshl_add_u64 v[14:15], s[4:5], 4, v[130:131]
	s_ashr_i32 s5, s4, 31
	s_lshl_b64 s[4:5], s[4:5], 4
	global_load_dwordx4 v[82:85], v[12:13], off offset:2048
	global_load_dwordx4 v[62:65], v[14:15], off
	v_lshl_add_u64 v[12:13], v[130:131], 0, s[4:5]
	s_addk_i32 s2, 0x1800
	v_lshl_add_u64 v[14:15], v[132:133], 0, s[4:5]
	global_load_dwordx4 v[66:69], v[12:13], off offset:1024
	global_load_dwordx4 v[70:73], v[14:15], off offset:2048
	v_lshl_add_u64 v[12:13], s[2:3], 4, v[130:131]
	s_ashr_i32 s3, s2, 31
	s_lshl_b64 s[2:3], s[2:3], 4
	v_lshl_add_u64 v[14:15], v[130:131], 0, s[2:3]
	global_load_dwordx4 v[50:53], v[12:13], off
	global_load_dwordx4 v[54:57], v[14:15], off offset:1024
	v_lshl_add_u64 v[12:13], v[132:133], 0, s[2:3]
	global_load_dwordx4 v[58:61], v[12:13], off offset:2048
	s_mul_i32 s26, s23, 0x840
	v_add_u32_e32 v20, s26, v20
	v_add_u32_e32 v22, s26, v22
	s_waitcnt vmcnt(15)
	ds_write_b128 v20, v[24:27]
	ds_write_b128 v20, v[32:35] offset:16896
	ds_write_b128 v20, v[40:43] offset:33792
	ds_write_b128 v20, v[102:105] offset:50688
	s_mov_b64 exec, s[18:19]
	ds_write_b128 v22, v[28:31]
	ds_write_b128 v22, v[36:39] offset:16896
	ds_write_b128 v22, v[44:47] offset:33792
	ds_write_b128 v22, v[106:109] offset:50688
	s_mov_b64 exec, -1
	s_cmp_gt_u32 s23, 3
	s_cbranch_scc1 .Lmy_conv_nor5
	v_add_u32_e32 v20, 0x10800, v20
	v_add_u32_e32 v22, 0x10800, v22
	ds_write_b128 v20, v[110:113]
	s_mov_b64 exec, s[18:19]
	ds_write_b128 v22, v[114:117]
	s_mov_b64 exec, -1
.Lmy_conv_nor5:
	s_waitcnt lgkmcnt(0)
	s_min_u32 s2, s23, 0x5e
	s_mulk_i32 s2, 0xc00
	s_mov_b32 s19, 0
	s_add_i32 s18, s2, 0x1e000
	v_lshl_add_u64 v[10:11], v[130:131], 0, s[18:19]
	v_lshl_add_u64 v[12:13], v[132:133], 0, s[18:19]
	s_barrier
	global_load_dwordx4 v[102:105], v[10:11], off
	global_load_dwordx4 v[106:109], v[10:11], off offset:1024
	global_load_dwordx4 v[110:113], v[12:13], off offset:2048
	v_and_b32_e32 v11, 3, v0
	v_bfe_u32 v12, v0, 2, 2
	s_mov_b32 s4, 0xf800000
	v_mad_u32_u24 v11, v11, 6, v12
	v_and_b32_e32 v10, 48, v0
	s_movk_i32 s18, 0x160
	v_mad_u32_u24 v150, v11, s18, v10
	v_add_f32_e32 v12, 0x3727c5ac, v164
	v_mul_f32_e32 v14, 0x4f800000, v12
	v_cmp_gt_f32_e32 vcc, s4, v12
	v_add_f32_e32 v13, 0x3727c5ac, v165
	v_mul_f32_e32 v15, 0x4f800000, v13
	v_cndmask_b32_e32 v147, v12, v14, vcc
	v_cmp_gt_f32_e64 s[2:3], s4, v13
	v_add_f32_e32 v12, 0x3727c5ac, v166
	v_cmp_gt_f32_e64 s[4:5], s4, v12
	v_cndmask_b32_e64 v148, v13, v15, s[2:3]
	v_mul_f32_e32 v13, 0x4f800000, v12
	v_sqrt_f32_e32 v154, v147
	v_cndmask_b32_e64 v149, v12, v13, s[4:5]
	v_sqrt_f32_e32 v155, v148
	v_sqrt_f32_e32 v156, v149
	v_add_u32_e32 v157, -1, v154
	v_add_u32_e32 v151, 1, v154
	v_add_u32_e32 v158, -1, v155
	v_add_u32_e32 v152, 1, v155
	v_fma_f32 v12, -v157, v154, v147
	v_fma_f32 v13, -v151, v154, v147
	v_add_u32_e32 v159, -1, v156
	v_add_u32_e32 v153, 1, v156
	v_fma_f32 v14, -v158, v155, v148
	v_fma_f32 v15, -v152, v155, v148
	v_cmp_ge_f32_e64 s[12:13], 0, v12
	v_cmp_lt_f32_e64 s[6:7], 0, v13
	v_fma_f32 v12, -v159, v156, v149
	v_fma_f32 v13, -v153, v156, v149
	v_cmp_ge_f32_e64 s[14:15], 0, v14
	v_cmp_lt_f32_e64 s[8:9], 0, v15
	v_cmp_ge_f32_e64 s[16:17], 0, v12
	v_cmp_lt_f32_e64 s[10:11], 0, v13
	s_cmpk_gt_u32 s24, 0x21bf
	s_cbranch_scc1 .LBB0_24
	s_mul_i32 s27, s23, 0x6d
	s_lshr_b32 s28, s27, 8
	s_sub_i32 s28, s23, s28
	s_bfe_u32 s28, s28, 0x70001
	s_bfe_u32 s27, s27, 0x80008
	s_add_i32 s28, s28, s27
	s_bfe_u32 s27, s28, 0x30005
	s_mul_i32 s28, s23, 0x89
	s_bfe_u32 s28, s28, 0x5000b
	s_mul_i32 s29, s28, 0x56
	s_mul_i32 s18, s23, 0xcd
	s_bfe_u32 s29, s29, 0x80008
	s_bfe_u32 s18, s18, 0x6000a
	s_mul_i32 s29, s29, 3
	s_sub_i32 s28, s28, s29
	s_mul_i32 s29, s18, 0x56
	s_bfe_u32 s29, s29, 0x80008
	s_mul_i32 s29, s29, 3
	s_mul_i32 s26, s18, -5
	s_sub_i32 s18, s18, s29
	s_mul_i32 s27, s27, 36
	s_mul_i32 s28, s28, 6
	s_or_b32 s18, s18, s27
	s_add_i32 s18, s18, s28
	s_add_i32 s26, s26, s23
	s_and_b32 s18, s18, 0xff
	s_mulk_i32 s18, 0x160
	s_lshl_b32 s26, s26, 6
	s_add_i32 s26, s26, s18
	v_add_u32_e32 v14, s26, v150
	ds_read_b128 v[10:13], v14
	ds_read_b128 v[114:117], v14 offset:38016
	s_waitcnt lgkmcnt(1)
	v_mfma_f32_16x16x32_f16 v[46:49], v[10:13], v[2:5], 0
	v_mfma_f32_16x16x32_f16 v[42:45], v[10:13], v[6:9], 0
	v_mfma_f32_16x16x32_f16 v[34:37], v[10:13], v[98:101], 0
	ds_read_b128 v[10:13], v14 offset:12672
	ds_read_b128 v[14:17], v14 offset:25344
	s_waitcnt lgkmcnt(1)
	v_mfma_f32_16x16x32_f16 v[38:41], v[10:13], v[2:5], 0
	v_mfma_f32_16x16x32_f16 v[30:33], v[10:13], v[6:9], 0
	v_mfma_f32_16x16x32_f16 v[26:29], v[10:13], v[98:101], 0
	s_waitcnt lgkmcnt(0)
	v_mfma_f32_16x16x32_f16 v[22:25], v[14:17], v[2:5], 0
	v_mfma_f32_16x16x32_f16 v[18:21], v[14:17], v[6:9], 0
	v_mfma_f32_16x16x32_f16 v[14:17], v[14:17], v[98:101], 0
	v_mfma_f32_16x16x32_f16 v[10:13], v[114:117], v[2:5], 0
	v_mfma_f32_16x16x32_f16 v[6:9], v[114:117], v[6:9], 0
	v_mfma_f32_16x16x32_f16 v[2:5], v[114:117], v[98:101], 0
	s_branch .LBB0_25

	.amdhsa_kernel _Z11k_conv_mfmaPKDF16_PKDv8_DF16_PKfS5_S5_S5_S5_PDF16_
		.amdhsa_group_segment_fixed_size 98304
		.amdhsa_private_segment_fixed_size 0
		.amdhsa_kernarg_size 64
		.amdhsa_user_sgpr_count 2
		.amdhsa_user_sgpr_dispatch_ptr 0
		.amdhsa_user_sgpr_queue_ptr 0
		.amdhsa_user_sgpr_kernarg_segment_ptr 1
		.amdhsa_user_sgpr_dispatch_id 0
		.amdhsa_user_sgpr_kernarg_preload_length 0
		.amdhsa_user_sgpr_kernarg_preload_offset 0
		.amdhsa_user_sgpr_private_segment_size 0
		.amdhsa_uses_dynamic_stack 0
		.amdhsa_enable_private_segment 0
		.amdhsa_system_sgpr_workgroup_id_x 1
		.amdhsa_system_sgpr_workgroup_id_y 0
		.amdhsa_system_sgpr_workgroup_id_z 0
		.amdhsa_system_sgpr_workgroup_info 0
		.amdhsa_system_vgpr_workitem_id 0
		.amdhsa_next_free_vgpr 173
		.amdhsa_next_free_sgpr 96
		.amdhsa_accum_offset 168
		.amdhsa_reserve_vcc 1
		.amdhsa_float_round_mode_32 0
		.amdhsa_float_round_mode_16_64 0
		.amdhsa_float_denorm_mode_32 3
		.amdhsa_float_denorm_mode_16_64 3
		.amdhsa_dx10_clamp 1
		.amdhsa_ieee_mode 1
		.amdhsa_fp16_overflow 0
		.amdhsa_tg_split 0
		.amdhsa_exception_fp_ieee_invalid_op 0
		.amdhsa_exception_fp_denorm_src 0
		.amdhsa_exception_fp_ieee_div_zero 0
		.amdhsa_exception_fp_ieee_overflow 0
		.amdhsa_exception_fp_ieee_underflow 0
		.amdhsa_exception_fp_ieee_inexact 0
		.amdhsa_exception_int_div_zero 0
	.end_amdhsa_kernel

amdhsa.kernels:
  - .agpr_count:     0
    .args:
      - .actual_access:  read_only
        .address_space:  global
        .offset:         0
        .size:           8
        .value_kind:     global_buffer
      - .actual_access:  read_only
        .address_space:  global
        .offset:         8
        .size:           8
        .value_kind:     global_buffer
      - .actual_access:  read_only
        .address_space:  global
        .offset:         16
        .size:           8
        .value_kind:     global_buffer
      - .actual_access:  read_only
        .address_space:  global
        .offset:         24
        .size:           8
        .value_kind:     global_buffer
      - .actual_access:  read_only
        .address_space:  global
        .offset:         32
        .size:           8
        .value_kind:     global_buffer
      - .actual_access:  read_only
        .address_space:  global
        .offset:         40
        .size:           8
        .value_kind:     global_buffer
      - .actual_access:  read_only
        .address_space:  global
        .offset:         48
        .size:           8
        .value_kind:     global_buffer
      - .actual_access:  write_only
        .address_space:  global
        .offset:         56
        .size:           8
        .value_kind:     global_buffer
    .group_segment_fixed_size: 98304
    .kernarg_segment_align: 8
    .kernarg_segment_size: 64
    .language:       OpenCL C
    .language_version:
      - 2
      - 0
    .max_flat_workgroup_size: 512
    .name:           _Z11k_conv_mfmaPKDF16_PKDv8_DF16_PKfS5_S5_S5_S5_PDF16_
    .private_segment_fixed_size: 0
    .sgpr_count:     36
    .sgpr_spill_count: 0
    .symbol:         _Z11k_conv_mfmaPKDF16_PKDv8_DF16_PKfS5_S5_S5_S5_PDF16_.kd
    .uniform_work_group_size: 1
    .uses_dynamic_stack: false
    .vgpr_count:     173
    .vgpr_spill_count: 0
    .wavefront_size: 64
  - .agpr_count:     0
    .args:
      - .actual_access:  read_only
        .address_space:  global
        .offset:         0
        .size:           8
        .value_kind:     global_buffer
      - .actual_access:  read_only
        .address_space:  global
        .offset:         8
        .size:           8
        .value_kind:     global_buffer
      - .actual_access:  read_only
        .address_space:  global
        .offset:         16
        .size:           8
        .value_kind:     global_buffer
      - .actual_access:  write_only
        .address_space:  global
        .offset:         24
        .size:           8
        .value_kind:     global_buffer
    .group_segment_fixed_size: 25600
    .kernarg_segment_align: 8
    .kernarg_segment_size: 32
    .language:       OpenCL C
    .language_version:
      - 2
      - 0
    .max_flat_workgroup_size: 1024
    .name:           _Z12k_recon_mfmaPKDF16_PKDv8_DF16_PKfPf
    .private_segment_fixed_size: 0
    .sgpr_count:     25
    .sgpr_spill_count: 0
    .symbol:         _Z12k_recon_mfmaPKDF16_PKDv8_DF16_PKfPf.kd
    .uniform_work_group_size: 1
    .uses_dynamic_stack: false
    .vgpr_count:     84
    .vgpr_spill_count: 0
    .wavefront_size: 64
  - .agpr_count:     0
    .args:
      - .actual_access:  read_only
        .address_space:  global
        .offset:         0
        .size:           8
        .value_kind:     global_buffer
      - .actual_access:  read_only
        .address_space:  global
        .offset:         8
        .size:           8
        .value_kind:     global_buffer
      - .actual_access:  read_only
        .address_space:  global
        .offset:         16
        .size:           8
        .value_kind:     global_buffer
      - .actual_access:  write_only
        .address_space:  global
        .offset:         24
        .size:           8
        .value_kind:     global_buffer
      - .actual_access:  write_only
        .address_space:  global
        .offset:         32
        .size:           8
        .value_kind:     global_buffer
      - .actual_access:  write_only
        .address_space:  global
        .offset:         40
        .size:           8
        .value_kind:     global_buffer
      - .actual_access:  write_only
        .address_space:  global
        .offset:         48
        .size:           8
        .value_kind:     global_buffer
      - .actual_access:  write_only
        .address_space:  global
        .offset:         56
        .size:           8
        .value_kind:     global_buffer
      - .actual_access:  write_only
        .address_space:  global
        .offset:         64
        .size:           8
        .value_kind:     global_buffer
    .group_segment_fixed_size: 67600
    .kernarg_segment_align: 8
    .kernarg_segment_size: 72
    .language:       OpenCL C
    .language_version:
      - 2
      - 0
    .max_flat_workgroup_size: 512
    .name:           _Z11k_proj_mfmaPKDF16_PKDv8_DF16_PKfPfPS1_S6_PhS6_PDF16_
    .private_segment_fixed_size: 0
    .sgpr_count:     36
    .sgpr_spill_count: 0
    .symbol:         _Z11k_proj_mfmaPKDF16_PKDv8_DF16_PKfPfPS1_S6_PhS6_PDF16_.kd
    .uniform_work_group_size: 1
    .uses_dynamic_stack: false
    .vgpr_count:     155
    .vgpr_spill_count: 0
    .wavefront_size: 64
  - .agpr_count:     0
    .args:
      - .actual_access:  read_only
        .address_space:  global
        .offset:         0
        .size:           8
        .value_kind:     global_buffer
      - .actual_access:  read_only
        .address_space:  global
        .offset:         8
        .size:           8
        .value_kind:     global_buffer
      - .actual_access:  read_only
        .address_space:  global
        .offset:         16
        .size:           8
        .value_kind:     global_buffer
      - .actual_access:  read_only
        .address_space:  global
        .offset:         24
        .size:           8
        .value_kind:     global_buffer
      - .actual_access:  read_only
        .address_space:  global
        .offset:         32
        .size:           8
        .value_kind:     global_buffer
      - .actual_access:  read_only
        .address_space:  global
        .offset:         40
        .size:           8
        .value_kind:     global_buffer
      - .actual_access:  write_only
        .address_space:  global
        .offset:         48
        .size:           8
        .value_kind:     global_buffer
      - .actual_access:  write_only
        .address_space:  global
        .offset:         56
        .size:           8
        .value_kind:     global_buffer
      - .actual_access:  read_only
        .address_space:  global
        .offset:         64
        .size:           8
        .value_kind:     global_buffer
      - .actual_access:  read_only
        .address_space:  global
        .offset:         72
        .size:           8
        .value_kind:     global_buffer
      - .actual_access:  write_only
        .address_space:  global
        .offset:         80
        .size:           8
        .value_kind:     global_buffer
      - .actual_access:  write_only
        .address_space:  global
        .offset:         88
        .size:           8
        .value_kind:     global_buffer
    .group_segment_fixed_size: 65536
    .kernarg_segment_align: 8
    .kernarg_segment_size: 96
    .language:       OpenCL C
    .language_version:
      - 2
      - 0
    .max_flat_workgroup_size: 512
    .name:           _Z6k_attnPKDv8_DF16_PKfPKhS3_S3_S3_PfS6_S3_S3_PS_S7_
    .private_segment_fixed_size: 0
    .sgpr_count:     34
    .sgpr_spill_count: 0
    .symbol:         _Z6k_attnPKDv8_DF16_PKfPKhS3_S3_S3_PfS6_S3_S3_PS_S7_.kd
    .uniform_work_group_size: 1
    .uses_dynamic_stack: false
    .vgpr_count:     126
    .vgpr_spill_count: 0
    .wavefront_size: 64
  - .agpr_count:     8
    .args:
      - .actual_access:  read_only
        .address_space:  global
        .offset:         0
        .size:           8
        .value_kind:     global_buffer
      - .actual_access:  read_only
        .address_space:  global
        .offset:         8
        .size:           8
        .value_kind:     global_buffer
      - .actual_access:  read_only
        .address_space:  global
        .offset:         16
        .size:           8
        .value_kind:     global_buffer
      - .actual_access:  read_only
        .address_space:  global
        .offset:         24
        .size:           8
        .value_kind:     global_buffer
      - .actual_access:  read_only
        .address_space:  global
        .offset:         32
        .size:           8
        .value_kind:     global_buffer
      - .actual_access:  write_only
        .address_space:  global
        .offset:         40
        .size:           8
        .value_kind:     global_buffer
    .group_segment_fixed_size: 10560
    .kernarg_segment_align: 8
    .kernarg_segment_size: 48
    .language:       OpenCL C
    .language_version:
      - 2
      - 0
    .max_flat_workgroup_size: 256
    .name:           _Z8k_resid2PKDF16_PKfS0_S2_S2_PDF16_
    .private_segment_fixed_size: 0
    .sgpr_count:     38
    .sgpr_spill_count: 0
    .symbol:         _Z8k_resid2PKDF16_PKfS0_S2_S2_PDF16_.kd
    .uniform_work_group_size: 1
    .uses_dynamic_stack: false
    .vgpr_count:     120
    .vgpr_spill_count: 0
    .wavefront_size: 64
  - .agpr_count:     0
    .args:
      - .actual_access:  read_only
        .address_space:  global
        .offset:         0
        .size:           8
        .value_kind:     global_buffer
      - .actual_access:  read_only
        .address_space:  global
        .offset:         8
        .size:           8
        .value_kind:     global_buffer
      - .actual_access:  read_only
        .address_space:  global
        .offset:         16
        .size:           8
        .value_kind:     global_buffer
      - .actual_access:  read_only
        .address_space:  global
        .offset:         24
        .size:           8
        .value_kind:     global_buffer
      - .actual_access:  read_only
        .address_space:  global
        .offset:         32
        .size:           8
        .value_kind:     global_buffer
      - .actual_access:  read_only
        .address_space:  global
        .offset:         40
        .size:           8
        .value_kind:     global_buffer
      - .actual_access:  read_only
        .address_space:  global
        .offset:         48
        .size:           8
        .value_kind:     global_buffer
      - .actual_access:  read_only
        .address_space:  global
        .offset:         56
        .size:           8
        .value_kind:     global_buffer
      - .actual_access:  read_only
        .address_space:  global
        .offset:         64
        .size:           8
        .value_kind:     global_buffer
      - .actual_access:  read_only
        .address_space:  global
        .offset:         72
        .size:           8
        .value_kind:     global_buffer
      - .actual_access:  write_only
        .address_space:  global
        .offset:         80
        .size:           8
        .value_kind:     global_buffer
      - .actual_access:  read_only
        .address_space:  global
        .offset:         88
        .size:           8
        .value_kind:     global_buffer
      - .actual_access:  read_only
        .address_space:  global
        .offset:         96
        .size:           8
        .value_kind:     global_buffer
      - .actual_access:  read_only
        .address_space:  global
        .offset:         104
        .size:           8
        .value_kind:     global_buffer
      - .actual_access:  read_only
        .address_space:  global
        .offset:         112
        .size:           8
        .value_kind:     global_buffer
      - .actual_access:  read_only
        .address_space:  global
        .offset:         120
        .size:           8
        .value_kind:     global_buffer
      - .actual_access:  read_only
        .address_space:  global
        .offset:         128
        .size:           8
        .value_kind:     global_buffer
      - .actual_access:  write_only
        .address_space:  global
        .offset:         136
        .size:           8
        .value_kind:     global_buffer
    .group_segment_fixed_size: 21248
    .kernarg_segment_align: 8
    .kernarg_segment_size: 144
    .language:       OpenCL C
    .language_version:
      - 2
      - 0
    .max_flat_workgroup_size: 512
    .name:           _Z8k_embed2PKfS0_S0_S0_S0_S0_S0_S0_S0_S0_PDF16_S0_S0_S0_S0_S0_S0_PDv8_DF16_
    .private_segment_fixed_size: 0
    .sgpr_count:     37
    .sgpr_spill_count: 0
    .symbol:         _Z8k_embed2PKfS0_S0_S0_S0_S0_S0_S0_S0_S0_PDF16_S0_S0_S0_S0_S0_S0_PDv8_DF16_.kd
    .uniform_work_group_size: 1
    .uses_dynamic_stack: false
    .vgpr_count:     99
    .vgpr_spill_count: 0
    .wavefront_size: 64
